# sliding-window unit: sink-term query positions requested in the unit prologue; next-unit ticket kept in flight over the epilogue
# baseline (speedup 1.0000x reference)
; __device__ __forceinline__ void claim_fire(unsigned* ctr, int tid, int* pend) { if (tid == 0) *pend = (int)__hip_atomic_fetch_add(ctr, 1u, __ATOMIC_RELAXED, __HIP_MEMORY_SCOPE_AGENT); }
;     ...
;     unsigned* q2ctr = F.ctl + CW_QUEUE + ((l + qlo) * 8 + 2 + qs) * 64; unsigned* q3ctr = F.ctl + CW_QUEUE + ((l + qlo) * 8 + 3 + qs) * 64;
;     const float* slopes8 = (const float*)(F.ctl + CW_LAM) + 16; const float* sinks = a->in[7] + l * 8;
;     at::claim_fire(q3ctr, F.tid, &pend);
.LBB0_1019:
	s_add_u32 s14, s52, 0x200
	s_addc_u32 s15, s53, 0
	v_writelane_b32 v255, s14, 3
	s_nop 1
	v_writelane_b32 v255, s15, 4
	s_and_saveexec_b64 s[14:15], s[38:39]
	s_cbranch_execz .LBB0_1023
	s_mov_b64 s[34:35], exec
	v_mbcnt_lo_u32_b32 v0, s34, 0
	v_mbcnt_hi_u32_b32 v0, s35, v0
	v_cmp_eq_u32_e32 vcc, 0, v0
	s_and_saveexec_b64 s[16:17], vcc
	s_cbranch_execz .LBB0_1022
	s_bcnt1_i32_b64 s3, s[34:35]
	v_readlane_b32 s20, v255, 3
	v_mov_b32_e32 v1, s3
	v_readlane_b32 s21, v255, 4
	s_nop 4
	global_atomic_add v1, v31, v1, s[20:21] sc0
.LBB0_1022:
	s_or_b64 exec, exec, s[16:17]
	s_waitcnt vmcnt(0)
	v_readfirstlane_b32 s3, v1
	s_nop 1
	v_add_u32_e32 v164, s3, v0
	v_mov_b32_e32 v192, v164
.LBB0_1023:
	s_or_b64 exec, exec, s[14:15]
	s_lshl_b32 s14, s72, 3
	s_ashr_i32 s15, s14, 31
	s_lshl_b64 s[14:15], s[14:15], 2
	s_add_u32 s3, s10, s14
	s_addc_u32 s4, s11, s15
	v_readlane_b32 s14, v254, 58
	s_add_u32 s10, s50, s14
	s_addc_u32 s11, s51, 0
	s_add_u32 s10, s10, 0x2040
	s_addc_u32 s11, s11, 0
	s_add_u32 s34, s3, s14
	v_readlane_b32 s14, v255, 3
	s_addc_u32 s35, s4, 0
	v_readlane_b32 s15, v255, 4
	s_cmp_lg_u64 s[14:15], 0
	s_cselect_b64 s[14:15], -1, 0
	s_mov_b64 s[24:25], s[72:73]
	s_branch .LBB0_1027

; #define LAS __attribute__((address_space(3)))
; __device__ __forceinline__ unsigned cvt_pk_bf16(float lo, float hi) { f32x2 v = {lo, hi}; bf16x2_t b = __builtin_convertvector(v, bf16x2_t); return __builtin_bit_cast(unsigned, b); }
;     ...
;     l = swapsum(l);
;     if (SWA) { const float sk = sink_l2 + (ALIBI ? slope_l2 * (float)(pos[qidx] - pos_ref) : 0.f);
;         const float mnew = fmaxf(m, sk), f = __builtin_amdgcn_exp2f(m - mnew); l = l * f + __builtin_amdgcn_exp2f(sk - mnew);
; #pragma unroll
;         for (int i = 0; i < 16; ++i) { ot[0][i] *= f; ot[1][i] *= f; } }
;     const float inv = 1.f / l;
;     if (MODE == 3) {
;         LAS float* xch = (LAS float*)(lds + XCH) + wq * 64 + lane;
;         if (mp) {
; #pragma unroll
;             for (int i = 0; i < 32; ++i) xch[i * 256] = ot[i >> 4][i & 15] * inv; }
;         lds_barrier();
;         if (!mp) {
;             float o[32]; float ss = 0.f;
; #pragma unroll
;             for (int i = 0; i < 32; ++i) { o[i] = ot[i >> 4][i & 15] * inv - lam * xch[i * 256]; ss += o[i] * o[i]; }
;             const float rs = __builtin_amdgcn_rsqf(swapsum(ss) * (1.f / 64.f) + 1e-6f);
;             bf16_t* op = (bf16_t*)outp + (size_t)qidx * opitch + 4 * hf;
; #pragma unroll
;             for (int db = 0; db < 2; ++db)
; #pragma unroll
;                 for (int g = 0; g < 4; ++g) { const f32x4 gn = *(const f32x4*)(gain + 32 * db + 8 * g + 4 * hf); const int i0 = 16 * db + 4 * g;
;                     *(u32x2*)(op + 32 * db + 8 * g) = (u32x2){cvt_pk_bf16(o[i0] * rs * gn[0], o[i0 + 1] * rs * gn[1]), cvt_pk_bf16(o[i0 + 2] * rs * gn[2], o[i0 + 3] * rs * gn[3])}; }
;         }
;     } else
;     if (F32OUT) { float* op = (float*)outp + (size_t)qidx * opitch + 4 * hf;
; #pragma unroll
;         for (int db = 0; db < 2; ++db)
; #pragma unroll
;             for (int g = 0; g < 4; ++g) *(f32x4*)(op + 32 * db + 8 * g) = (f32x4){ot[db][4 * g] * inv, ot[db][4 * g + 1] * inv, ot[db][4 * g + 2] * inv, ot[db][4 * g + 3] * inv}; }
;     else { bf16_t* op = (bf16_t*)outp + (size_t)qidx * opitch + 4 * hf + hsel * 64;
; #pragma unroll
;         for (int db = 0; db < 2; ++db)
; #pragma unroll
;             for (int g = 0; g < 4; ++g) *(u32x2*)(op + 32 * db + 8 * g) = (u32x2){cvt_pk_bf16(ot[db][4 * g] * inv, ot[db][4 * g + 1] * inv), cvt_pk_bf16(ot[db][4 * g + 2] * inv, ot[db][4 * g + 3] * inv)}; }
.LBB0_1025:
	s_or_b64 exec, exec, s[40:41]
	s_mulk_i32 s62, 0xa00
	v_mov_b32_e32 v2, v119
	s_add_u32 s3, s13, s62
	s_nop 0
	v_permlane32_swap_b32_e32 v119, v2
	s_addc_u32 s28, s31, 0
	s_lshl_b32 s20, s21, 1
	s_add_u32 s20, s3, s20
	s_addc_u32 s21, s28, 0
	s_movk_i32 s3, 0xa00
	v_ashrrev_i32_e32 v117, 31, v116
	v_sub_u32_e32 v0, v194, v115
	v_cvt_f32_i32_e32 v251, v0
	v_mov_b32_e32 v115, v122
	v_pk_mul_f32 v[0:1], v[114:115], v[250:251]
	s_nop 0
	v_add_f32_e32 v0, v0, v1
	v_max_f32_e32 v1, v172, v172
	v_max_f32_e32 v1, v1, v0
	v_sub_f32_e32 v3, v172, v1
	v_sub_f32_e32 v0, v0, v1
	v_exp_f32_e32 v4, v3
	v_exp_f32_e32 v0, v0
	v_add_f32_e32 v1, v119, v2
	v_fmac_f32_e32 v0, v1, v4
	v_div_scale_f32 v1, s[28:29], v0, v0, 1.0
	v_rcp_f32_e32 v2, v1
	s_nop 0
	v_fma_f32 v3, -v1, v2, 1.0
	v_fmac_f32_e32 v2, v3, v2
	v_div_scale_f32 v3, vcc, 1.0, v0, 1.0
	v_mul_f32_e32 v5, v3, v2
	v_fma_f32 v6, -v1, v5, v3
	v_fmac_f32_e32 v5, v6, v2
	v_fma_f32 v1, -v1, v5, v3
	v_div_fmas_f32 v1, v1, v2, v5
	v_mov_b64_e32 v[2:3], s[20:21]
	v_div_fixup_f32 v0, v1, v0, 1.0
	v_mad_i64_i32 v[2:3], s[20:21], v112, s3, v[2:3]
	v_pk_mul_f32 v[6:7], v[48:49], v[4:5] op_sel_hi:[1,0]
	v_pk_mul_f32 v[8:9], v[50:51], v[4:5] op_sel_hi:[1,0]
	v_lshl_add_u64 v[2:3], v[116:117], 1, v[2:3]
	v_pk_mul_f32 v[6:7], v[6:7], v[0:1] op_sel_hi:[1,0]
	v_pk_mul_f32 v[8:9], v[8:9], v[0:1] op_sel_hi:[1,0]
	v_lshl_add_u64 v[2:3], v[2:3], 0, s[4:5]
	v_cvt_pk_bf16_f32 v48, v6, v7
	v_cvt_pk_bf16_f32 v49, v8, v9
	v_pk_mul_f32 v[6:7], v[52:53], v[4:5] op_sel_hi:[1,0]
	v_pk_mul_f32 v[8:9], v[54:55], v[4:5] op_sel_hi:[1,0]
	v_pk_mul_f32 v[6:7], v[6:7], v[0:1] op_sel_hi:[1,0]
	v_pk_mul_f32 v[8:9], v[8:9], v[0:1] op_sel_hi:[1,0]
	v_cvt_pk_bf16_f32 v52, v6, v7
	v_cvt_pk_bf16_f32 v53, v8, v9
	v_pk_mul_f32 v[6:7], v[56:57], v[4:5] op_sel_hi:[1,0]
	v_pk_mul_f32 v[8:9], v[58:59], v[4:5] op_sel_hi:[1,0]
	v_pk_mul_f32 v[6:7], v[6:7], v[0:1] op_sel_hi:[1,0]
	v_pk_mul_f32 v[8:9], v[8:9], v[0:1] op_sel_hi:[1,0]
	v_cvt_pk_bf16_f32 v56, v6, v7
	v_cvt_pk_bf16_f32 v57, v8, v9
	v_pk_mul_f32 v[6:7], v[60:61], v[4:5] op_sel_hi:[1,0]
	v_pk_mul_f32 v[8:9], v[62:63], v[4:5] op_sel_hi:[1,0]
	v_pk_mul_f32 v[6:7], v[6:7], v[0:1] op_sel_hi:[1,0]
	v_pk_mul_f32 v[8:9], v[8:9], v[0:1] op_sel_hi:[1,0]
	v_cvt_pk_bf16_f32 v60, v6, v7
	v_cvt_pk_bf16_f32 v61, v8, v9
	v_pk_mul_f32 v[6:7], v[32:33], v[4:5] op_sel_hi:[1,0]
	v_pk_mul_f32 v[8:9], v[34:35], v[4:5] op_sel_hi:[1,0]
	v_pk_mul_f32 v[6:7], v[6:7], v[0:1] op_sel_hi:[1,0]
	v_pk_mul_f32 v[8:9], v[8:9], v[0:1] op_sel_hi:[1,0]
	v_cvt_pk_bf16_f32 v50, v6, v7
	v_cvt_pk_bf16_f32 v51, v8, v9
	v_pk_mul_f32 v[6:7], v[36:37], v[4:5] op_sel_hi:[1,0]
	v_pk_mul_f32 v[8:9], v[38:39], v[4:5] op_sel_hi:[1,0]
	v_pk_mul_f32 v[6:7], v[6:7], v[0:1] op_sel_hi:[1,0]
	v_pk_mul_f32 v[8:9], v[8:9], v[0:1] op_sel_hi:[1,0]
	v_cvt_pk_bf16_f32 v54, v6, v7
	v_cvt_pk_bf16_f32 v55, v8, v9
	v_pk_mul_f32 v[6:7], v[40:41], v[4:5] op_sel_hi:[1,0]
	v_pk_mul_f32 v[8:9], v[42:43], v[4:5] op_sel_hi:[1,0]
	v_pk_mul_f32 v[6:7], v[6:7], v[0:1] op_sel_hi:[1,0]
	v_pk_mul_f32 v[8:9], v[8:9], v[0:1] op_sel_hi:[1,0]
	v_cvt_pk_bf16_f32 v58, v6, v7
	v_cvt_pk_bf16_f32 v59, v8, v9
	v_pk_mul_f32 v[6:7], v[44:45], v[4:5] op_sel_hi:[1,0]
	v_pk_mul_f32 v[4:5], v[46:47], v[4:5] op_sel_hi:[1,0]
	v_pk_mul_f32 v[6:7], v[6:7], v[0:1] op_sel_hi:[1,0]
	v_pk_mul_f32 v[0:1], v[4:5], v[0:1] op_sel_hi:[1,0]
	v_cvt_pk_bf16_f32 v62, v6, v7
	v_cvt_pk_bf16_f32 v63, v0, v1
	s_nop 1
	v_permlane32_swap_b32_e32 v48, v50
	v_permlane32_swap_b32_e32 v49, v51
	v_permlane32_swap_b32_e32 v52, v54
	v_permlane32_swap_b32_e32 v53, v55
	v_permlane32_swap_b32_e32 v56, v58
	v_permlane32_swap_b32_e32 v57, v59
	v_permlane32_swap_b32_e32 v60, v62
	v_permlane32_swap_b32_e32 v61, v63
	v_mbcnt_lo_u32_b32 v8, -1, 0
	v_mbcnt_hi_u32_b32 v8, -1, v8
	v_lshrrev_b32_e32 v8, 5, v8
	v_mul_u32_u24_e32 v8, 56, v8
	v_add_co_u32_e32 v2, vcc, v2, v8
	s_nop 1
	v_addc_co_u32_e32 v3, vcc, 0, v3, vcc
	global_store_dwordx4 v[2:3], v[48:51], off offset:1024
	global_store_dwordx4 v[2:3], v[52:55], off offset:1040
	global_store_dwordx4 v[2:3], v[56:59], off offset:1056
	global_store_dwordx4 v[2:3], v[60:63], off offset:1072

; __device__ __forceinline__ int lane_id() { unsigned m = ~0u; asm volatile("" : "+s"(m)); return (int)__builtin_amdgcn_mbcnt_hi(m, __builtin_amdgcn_mbcnt_lo(m, 0u)); }
;     ...
;     const int tid = wv * 64 + lane, r32 = lane & 31, hf = lane >> 5;
;     const int wq = (MODE == 3) ? (wv & 3) : (MODE == 4) ? (wv & 1) : wv, mp = (MODE == 3) ? (wv >> 2) : 0, hsel = (MODE == 4) ? (wv >> 1) : 0;
;     if (MODE == 4) { slope_l2 = slp[hsel] * LOG2E; sink_l2 = snk[hsel] * LOG2E; }
;     const int qmin = q0 + 32 * wq, qidx = qmin + r32, qmax = qmin + 31;
;     int t_lo = 0; if (SWA) { t_lo = q0 - 127; t_lo = (t_lo < 0 ? 0 : t_lo) >> 7; }
;     const int t_hi = (q0 + ((MODE == 3) ? 127 : (MODE == 4) ? 63 : 255)) >> 7;
;     if (MODE == 3 && mp) kmax = kmax1;
;     const int pos_ref = ALIBI ? pos[q0] : 0;
;     bf16x8 qf[NC];
;     { const bf16_t* qr = T.q + (size_t)qidx * T.qp + 8 * hf + (mp + hsel) * DQK;
; #pragma unroll
;       for (int c = 0; c < NC; ++c) qf[c] = *(const bf16x8*)(qr + 16 * c); }
;     f32x16 ot[2];
; #pragma unroll
;     for (int i = 0; i < 16; ++i) { ot[0][i] = 0.f; ot[1][i] = 0.f; }
;     float m = SWA ? -1e30f : 0.f, l = 0.f; bool first = true;
;     u32x4 kreg[NKI], vreg[2]; float breg = 0.f;
;     const int vr = tid >> 3, vc = tid & 7;
;     ...
;     if (qmask & 8) for (;;) {
;         const int idx = at::claim_take(lds, F.tid, &pend); if (idx >= 512) break;
;         const int qb = idx >> 2, r = idx & 3, b = r >> 1, hk = r & 1;
;         const bf16_t* Hb = H + (size_t)b * S * HP;
;         at::Tens T{Hb + C_SWQ + hk * 256, Hb + C_SWKV + hk * 64, Hb + C_SWKV + 128 + hk * 64, HP, HP, HP};
;         at::softmax_unit<64, true, 4, false>(lds, wv, lane_id(), T, pos, qb * 64, 0.f, 0.f, O + (size_t)b * S * OP + 512 + hk * 256, OP, 0.f, nullptr, 0.f, 0.f, nullptr, q2ctr, &pend, slopes8 + 4 * hk, sinks + 4 * hk);
.LBB0_1027:
	s_and_saveexec_b64 s[16:17], s[38:39]
	s_waitcnt vmcnt(4)
	ds_write_b32 v247, v192
	s_or_b64 exec, exec, s[16:17]
	s_waitcnt lgkmcnt(0)
	s_barrier
	ds_read_b32 v0, v247
	s_waitcnt lgkmcnt(0)
	s_barrier
	s_waitcnt lgkmcnt(0)
	v_readfirstlane_b32 s20, v0
	s_cmpk_gt_i32 s20, 0x1ff
	s_cselect_b64 s[16:17], -1, 0
	s_and_b64 vcc, exec, s[16:17]
	s_cbranch_vccnz .LBB0_1026
	s_lshl_b32 s3, s20, 12
	s_and_b32 s62, s3, 0x2000
	s_and_b32 s21, s20, 1
	s_mul_i32 s3, s62, 0x1600
	s_add_u32 s3, s2, s3
	s_addc_u32 s4, s1, 0
	s_lshl_b32 s28, s21, 9
	s_add_u32 s28, s3, s28
	s_addc_u32 s29, s4, 0
	s_lshl_b32 s40, s21, 7
	s_add_u32 s42, s3, s40
	s_mov_b32 s3, -1
	s_addc_u32 s43, s4, 0
	v_mbcnt_lo_u32_b32 v0, s3, 0
	v_mbcnt_hi_u32_b32 v4, s3, v0
	s_lshl_b32 s3, s20, 4
	s_and_b32 s40, s3, 0xffffffc0
	s_lshl_b32 s3, s21, 4
	v_mov_b32_e32 v0, s3
	v_readlane_b32 s3, v254, 18
	v_and_b32_e32 v5, 31, v4
	s_or_b32 s63, s40, s3
	v_ashrrev_i32_e32 v6, 5, v4
	global_load_dword v7, v0, s[10:11]
	global_load_dword v114, v0, s[34:35]
	v_or_b32_e32 v112, s63, v5
	s_max_i32 s3, s40, 0x7f
	s_ashr_i32 s41, s40, 31
	v_mov_b64_e32 v[0:1], s[28:29]
	s_addk_i32 s3, 0xff81
	s_lshl_b64 s[40:41], s[40:41], 2
	v_mad_i64_i32 v[0:1], s[28:29], v112, s33, v[0:1]
	v_lshlrev_b32_e32 v2, 3, v6
	s_add_u32 s40, s6, s40
	v_ashrrev_i32_e32 v3, 31, v2
	v_readlane_b32 s4, v254, 19
	v_readlane_b32 s28, v254, 53
	s_addc_u32 s41, s7, s41
	v_lshl_add_u64 v[0:1], v[2:3], 1, v[0:1]
	s_lshl_b32 s4, s4, 1
	v_add_u32_e32 v118, s28, v4
	v_lshl_add_u64 v[0:1], v[0:1], 0, s[4:5]
	v_ashrrev_i32_e32 v119, 31, v118
	global_load_dword v115, v31, s[40:41]
	v_ashrrev_i32_e32 v195, 31, v112
	v_mov_b32_e32 v194, v112
	v_lshl_add_u64 v[194:195], v[194:195], 2, s[6:7]
	global_load_dword v194, v[194:195], off
	global_load_dwordx4 v[80:83], v[0:1], off offset:2368
	global_load_dwordx4 v[84:87], v[0:1], off offset:2400
	global_load_dwordx4 v[88:91], v[0:1], off offset:2432
	global_load_dwordx4 v[92:95], v[0:1], off offset:2464
	v_lshrrev_b32_e32 v0, 29, v119
	v_add_u32_e32 v0, v118, v0
	s_and_b32 s44, s3, 0xffffff80
	v_ashrrev_i32_e32 v8, 3, v0
	v_and_b32_e32 v0, -8, v0
	v_sub_u32_e32 v11, v118, v0
	v_add_u32_e32 v0, s44, v8
	v_mov_b64_e32 v[2:3], s[42:43]
	v_mad_i64_i32 v[12:13], s[28:29], v0, s33, v[2:3]
	v_lshlrev_b32_e32 v0, 3, v11
	v_ashrrev_i32_e32 v1, 31, v0
	v_lshl_add_u64 v[14:15], v[0:1], 1, v[12:13]
	v_add_u32_e32 v12, 0x200, v118
	v_ashrrev_i32_e32 v9, 31, v12
	v_lshrrev_b32_e32 v9, 29, v9
	v_add_u32_e32 v13, v12, v9
	v_ashrrev_i32_e32 v9, 3, v13
	v_and_b32_e32 v13, -8, v13
	v_and_b32_e32 v10, 7, v4
	v_sub_u32_e32 v12, v12, v13
	v_add_u32_e32 v13, s44, v9
	v_mad_i64_i32 v[16:17], s[28:29], v13, s33, v[2:3]
	v_lshlrev_b32_e32 v2, 3, v12
	v_ashrrev_i32_e32 v117, 3, v118
	v_lshlrev_b32_e32 v30, 4, v10
	v_ashrrev_i32_e32 v3, 31, v2
	v_add_u32_e32 v13, s44, v117
	v_lshl_add_u64 v[120:121], s[42:43], 0, v[30:31]
	v_lshl_add_u64 v[16:17], v[2:3], 1, v[16:17]
	global_load_dwordx4 v[96:99], v[14:15], off offset:3392
	global_load_dwordx4 v[100:103], v[16:17], off offset:3392
	v_mad_i64_i32 v[14:15], s[28:29], v13, s33, v[120:121]
	v_add_u32_e32 v13, 64, v13
	v_mad_i64_i32 v[16:17], s[28:29], v13, s33, v[120:121]
	global_load_dwordx4 v[104:107], v[14:15], off offset:3648
	global_load_dwordx4 v[108:111], v[16:17], off offset:3648
	s_movk_i32 s28, 0x80
	v_cmp_gt_i32_e64 s[40:41], s28, v118
	v_mov_b32_e32 v158, 0
	s_and_saveexec_b64 s[46:47], s[40:41]
	s_cbranch_execz .LBB0_1032
	v_add_u32_e32 v14, s44, v118
	v_ashrrev_i32_e32 v15, 31, v14
	v_lshl_add_u64 v[14:15], v[14:15], 2, s[6:7]
	global_load_dword v13, v[14:15], off
	s_waitcnt vmcnt(0)
	v_sub_u32_e32 v13, v13, v115
	v_cvt_f32_i32_e32 v158, v13

;     ...
;         if (!has_next || alldone) break;
;         t = tn; { const int tb_ = b0; b0 = b1; b1 = tb_; }
;     }
;     ...
;     if (nctr != nullptr && tid == 0) *pend = (int)__hip_atomic_fetch_add(nctr, 1u, __ATOMIC_RELAXED, __HIP_MEMORY_SCOPE_AGENT);
.LBB0_1065:
	v_cmp_eq_u32_e32 vcc, 0, v118
	s_and_b64 s[28:29], s[14:15], vcc
	s_and_saveexec_b64 s[40:41], s[28:29]
	v_readlane_b32 s92, v254, 59
	v_readlane_b32 s93, v254, 60
	v_readlane_b32 s95, v254, 61
	s_cbranch_execz .LBB0_1025
	s_mov_b64 s[44:45], exec
	v_mbcnt_lo_u32_b32 v0, s44, 0
	v_mbcnt_hi_u32_b32 v0, s45, v0
	v_cmp_eq_u32_e32 vcc, 0, v0
	s_and_saveexec_b64 s[42:43], vcc
	s_cbranch_execz .LBB0_1024
	s_bcnt1_i32_b64 s3, s[44:45]
	v_readlane_b32 s28, v255, 3
	v_mov_b32_e32 v1, s3
	v_readlane_b32 s29, v255, 4
	s_nop 4
	global_atomic_add v192, v31, v1, s[28:29] sc0
	s_branch .LBB0_1024
